# v91: R1 router-weight loads hoisted above the grid-barrier wait; final-phase POS/g_final loads overlapped with npan load
# baseline (speedup 1.0000x reference)
; __device__ __forceinline__ unsigned xb_add(unsigned* p, unsigned v) { return __hip_atomic_fetch_add(p, v, __ATOMIC_RELAXED, __HIP_MEMORY_SCOPE_AGENT); }
; __device__ __forceinline__ void xcd_barrier(const XcdBarrier& b) {
;     asm volatile("s_waitcnt vmcnt(0)" ::: "memory");
;     __syncthreads();
;     if (threadIdx.x == 0) {
;         unsigned* bar = b.bar;
;         __builtin_amdgcn_s_waitcnt(0);
;         unsigned nloc = b.st[0], nx = b.st[1];
;         if (nloc == 0u) { xcd_barrier_complete(bar, b.x, nloc, nx); b.st[0] = nloc; b.st[1] = nx; }
;         const unsigned old = xb_add(&bar[XB_XSUB(b.x)], 1u);
; template <int layer> __device__ __forceinline__ void layer_phases(const Ctx& c, unsigned char* lds) {
;     ...
;                 { f32x4 ra[2][2]; float gk[2];
; #pragma unroll
;                   for (int j = 0; j < 2; ++j) { const int k = tid + NTHR * j; ra[j][0] = *(const f32x4*)(args.moe_router + k * 8); ra[j][1] = *(const f32x4*)(args.moe_router + k * 8 + 4); gk[j] = gf[k]; }
.LBB0_1347:
	v_readlane_b32 s4, v254, 0
	v_readlane_b32 s5, v254, 1
	s_cmp_gt_i32 s5, 22
	s_cselect_b64 s[4:5], -1, 0
	s_and_b64 s[0:1], s[0:1], s[4:5]
	s_andn2_b64 vcc, exec, s[0:1]
	v_readlane_b32 s6, v254, 2
	v_readlane_b32 s7, v254, 3
	s_cbranch_vccnz .Lr1_stub
	s_waitcnt vmcnt(0)
	s_waitcnt lgkmcnt(0)
	s_barrier
	v_lshlrev_b32_e32 v96, 5, v0
	v_lshlrev_b32_e32 v97, 2, v0
	v_add_u32_e32 v98, 0x4000, v96
	v_add_u32_e32 v97, 0x1000, v97
	global_load_dwordx4 v[100:103], v96, s[50:51]
	global_load_dwordx4 v[104:107], v96, s[50:51] offset:16
	global_load_dword v108, v97, s[42:43]
	global_load_dword v109, v97, s[42:43] offset:2048
	global_load_dwordx4 v[110:113], v98, s[50:51]
	global_load_dwordx4 v[114:117], v98, s[50:51] offset:16
	s_mov_b64 s[0:1], exec
	v_readlane_b32 s2, v254, 7
	v_readlane_b32 s3, v254, 8
	s_and_b64 s[2:3], s[0:1], s[2:3]
	s_mov_b64 exec, s[2:3]
	s_cbranch_execz .LBB0_1400
	s_add_i32 s2, 0, 0x23960
	v_mov_b32_e32 v1, s2
	s_waitcnt vmcnt(0) expcnt(0) lgkmcnt(0)
	ds_read_b32 v3, v1
	s_add_i32 s2, 0, 0x23964
	v_mov_b32_e32 v1, s2
	ds_read_b32 v1, v1
	s_waitcnt lgkmcnt(1)
	v_cmp_ne_u32_e32 vcc, 0, v3
	s_cbranch_vccnz .LBB0_1364
	v_readlane_b32 s6, v254, 4
	v_readlane_b32 s7, v254, 5
	s_load_dwordx2 s[2:3], s[6:7], 0x4
	s_add_u32 s6, s90, 0x1000
	s_addc_u32 s7, s91, 0
	s_add_u32 s8, s90, 0x1100
	s_addc_u32 s9, s91, 0
	s_add_u32 s10, s90, 0x1200
	s_addc_u32 s11, s91, 0
	s_waitcnt lgkmcnt(0)
	s_mul_i32 s2, s2, s97
	s_add_u32 s12, s90, 0x1300
	s_mul_i32 s2, s2, s3
	s_addc_u32 s13, s91, 0
	s_mov_b32 s3, 1
	v_mov_b32_e32 v17, 0
	s_branch .LBB0_1352

; __device__ __forceinline__ void xcd_barrier(const XcdBarrier& b) {
;     ...
;     __syncthreads();
; template <int layer> __device__ __forceinline__ void layer_phases(const Ctx& c, unsigned char* lds) {
;     ...
;                 { f32x4 ra[2][2]; float gk[2];
; #pragma unroll
;                   for (int j = 0; j < 2; ++j) { const int k = tid + NTHR * j; ra[j][0] = *(const f32x4*)(args.moe_router + k * 8); ra[j][1] = *(const f32x4*)(args.moe_router + k * 8 + 4); gk[j] = gf[k]; }
; #pragma unroll
;                   for (int j = 0; j < 2; ++j) { const int k = tid + NTHR * j;
; #pragma unroll
;                       for (int e = 0; e < 4; ++e) { wr_l[e * D + k] = ra[j][0][e] * gk[j]; wr_l[(4 + e) * D + k] = ra[j][1][e] * gk[j]; } } }
;                 if (tid < 8) cnt_l[tid] = 0;
;                 __syncthreads();
;                 for (int blk = bx; blk < 256; blk += G) {
;                     if (blk != bx) { __syncthreads(); if (tid < 8) cnt_l[tid] = 0; __syncthreads(); }
;                     v4u xpre[8][2];
; #pragma unroll
;                     for (int i = 0; i < 8; ++i) { const v4u* xr = (const v4u*)(XB + (size_t)(blk * 64 + wave * 8 + i) * D) + lane; xpre[i][0] = xr[0]; xpre[i][1] = xr[64]; }
;                     const int mi = blk * 64 + wave * 8 + (lane >> 3);
;                     typedef float f32x2_t __attribute__((ext_vector_type(2))); const f32x2_t ssp = *(const f32x2_t*)(SS + (size_t)mi * 16 + 2 * (lane & 7));
.LBB0_1400:
	s_or_b64 exec, exec, s[0:1]
	s_waitcnt lgkmcnt(0)
	s_barrier
	s_branch .LBB0_1401
.Lr1_stub:
	v_lshlrev_b32_e32 v96, 5, v0
	v_lshlrev_b32_e32 v97, 2, v0
	v_add_u32_e32 v98, 0x4000, v96
	v_add_u32_e32 v97, 0x1000, v97
	global_load_dwordx4 v[100:103], v96, s[50:51]
	global_load_dwordx4 v[104:107], v96, s[50:51] offset:16
	global_load_dword v108, v97, s[42:43]
	global_load_dword v109, v97, s[42:43] offset:2048
	global_load_dwordx4 v[110:113], v98, s[50:51]
	global_load_dwordx4 v[114:117], v98, s[50:51] offset:16
.LBB0_1401:
	v_readlane_b32 s0, v254, 0
	v_readlane_b32 s1, v254, 1
	s_cmp_lt_i32 s0, 23
	s_cselect_b64 s[0:1], -1, 0
	s_add_u32 s22, s78, 0x300000
	s_addc_u32 s23, s79, 0
	s_add_u32 s24, s78, 0x320000
	s_addc_u32 s25, s79, 0
	s_add_u32 s26, s78, 0x360000
	s_addc_u32 s27, s79, 0
	v_readlane_b32 s2, v254, 2
	v_readlane_b32 s3, v254, 3
	s_add_u32 s28, s78, 0x370000
	s_addc_u32 s29, s79, 0
	s_and_b64 s[2:3], s[0:1], s[4:5]
	s_cmpk_lt_i32 s94, 0x100
	s_cselect_b64 s[30:31], -1, 0
	s_andn2_b64 vcc, exec, s[2:3]
	s_cbranch_vccnz .LBB0_1439
	s_waitcnt vmcnt(12)
	v_mov_b32_e32 v2, v0
	s_mov_b64 s[2:3], 0x1000
	v_ashrrev_i32_e32 v3, 31, v2
	s_waitcnt vmcnt(10)
	v_lshlrev_b32_e32 v12, 3, v2
	s_waitcnt vmcnt(9)
	v_lshl_add_u64 v[14:15], v[2:3], 2, s[42:43]
	v_ashrrev_i32_e32 v13, 31, v12
	v_add_co_u32_e32 v16, vcc, 0x1000, v14
	v_lshl_add_u64 v[8:9], v[12:13], 2, s[50:51]
	s_nop 0
	v_addc_co_u32_e32 v17, vcc, 0, v15, vcc
	v_add_u32_e32 v12, 0x1000, v12
	s_nop 0
	v_lshl_add_u64 v[14:15], v[14:15], 0, s[2:3]
	v_ashrrev_i32_e32 v13, 31, v12
	s_waitcnt vmcnt(11)
	v_lshl_add_u64 v[20:21], v[12:13], 2, s[50:51]
	s_nop 0
	v_lshl_add_u32 v1, v2, 2, 0
	v_cmp_gt_i32_e64 s[4:5], 8, v2
	s_waitcnt vmcnt(0)
	v_mov_b32_e32 v8, v100
	v_mov_b32_e32 v9, v101
	v_mov_b32_e32 v10, v102
	v_mov_b32_e32 v11, v103
	v_mov_b32_e32 v4, v104
	v_mov_b32_e32 v5, v105
	v_mov_b32_e32 v6, v106
	v_mov_b32_e32 v7, v107
	v_mov_b32_e32 v3, v108
	v_mov_b32_e32 v22, v109
	v_mov_b32_e32 v12, v110
	v_mov_b32_e32 v13, v111
	v_mov_b32_e32 v14, v112
	v_mov_b32_e32 v15, v113
	v_mov_b32_e32 v16, v114
	v_mov_b32_e32 v17, v115
	v_mov_b32_e32 v18, v116
	v_mov_b32_e32 v19, v117
	s_waitcnt vmcnt(3)
	v_mul_f32_e32 v8, v8, v3
	v_mul_f32_e32 v4, v3, v4
	v_mul_f32_e32 v9, v9, v3
	v_mul_f32_e32 v5, v3, v5
	v_mul_f32_e32 v10, v10, v3
	v_mul_f32_e32 v6, v3, v6
	v_mul_f32_e32 v11, v11, v3
	v_mul_f32_e32 v3, v3, v7
	s_waitcnt vmcnt(1)
	v_mul_f32_e32 v7, v12, v22
	s_waitcnt vmcnt(0)
	v_mul_f32_e32 v12, v22, v16
	v_mul_f32_e32 v13, v13, v22
	v_mul_f32_e32 v16, v22, v17
	v_mul_f32_e32 v14, v14, v22
	v_mul_f32_e32 v17, v22, v18
	v_mul_f32_e32 v15, v15, v22
	v_mul_f32_e32 v18, v22, v19
	ds_write2st64_b32 v1, v8, v7 offset1:8
	ds_write2st64_b32 v1, v4, v12 offset0:64 offset1:72
	ds_write2st64_b32 v1, v9, v13 offset0:16 offset1:24
	ds_write2st64_b32 v1, v5, v16 offset0:80 offset1:88
	ds_write2st64_b32 v1, v10, v14 offset0:32 offset1:40
	ds_write2st64_b32 v1, v6, v17 offset0:96 offset1:104
	ds_write2st64_b32 v1, v11, v15 offset0:48 offset1:56
	ds_write2st64_b32 v1, v3, v18 offset0:112 offset1:120
	s_and_saveexec_b64 s[6:7], s[4:5]
	v_mov_b32_e32 v3, 0
	ds_write_b32 v1, v3 offset:32768
	s_or_b64 exec, exec, s[6:7]
	s_andn2_b64 vcc, exec, s[30:31]
	s_waitcnt lgkmcnt(0)
	s_barrier
	s_cbranch_vccnz .LBB0_1439
	v_and_b32_e32 v4, 64, v228
	v_and_b32_e32 v3, 63, v2
	v_add_u32_e32 v4, 64, v4
	v_xor_b32_e32 v5, 1, v228
	v_lshlrev_b32_e32 v118, 4, v3
	v_mov_b32_e32 v119, 0
	v_and_b32_e32 v133, 7, v2
	v_cmp_lt_i32_e32 vcc, v5, v4
	v_lshl_add_u64 v[120:121], s[86:87], 0, v[118:119]
	v_lshlrev_b32_e32 v118, 3, v133
	v_cndmask_b32_e32 v5, v228, v5, vcc
	v_lshl_add_u64 v[122:123], s[80:81], 0, v[118:119]
	v_lshlrev_b32_e32 v118, 2, v5
	v_xor_b32_e32 v5, 2, v228
	v_cmp_lt_i32_e32 vcc, v5, v4
	v_readlane_b32 s20, v254, 10
	s_lshl_b32 s3, s96, 3
	v_cndmask_b32_e32 v5, v228, v5, vcc
	v_lshlrev_b32_e32 v134, 2, v5
	v_xor_b32_e32 v5, 4, v228
	v_cmp_lt_i32_e32 vcc, v5, v4
	v_add_u32_e32 v124, s20, v2
	s_lshl_b32 s20, s94, 6
	v_cndmask_b32_e32 v5, v228, v5, vcc
	v_lshlrev_b32_e32 v135, 2, v5
	v_and_b32_e32 v5, 32, v2
	v_cmp_eq_u32_e64 s[8:9], 0, v5
	v_xor_b32_e32 v5, 32, v228
	v_cmp_lt_i32_e32 vcc, v5, v4
	v_bfe_u32 v132, v2, 3, 3
	s_add_i32 s20, s20, s3
	v_cndmask_b32_e32 v5, v228, v5, vcc
	v_lshlrev_b32_e32 v136, 2, v5
	v_and_b32_e32 v5, 16, v2
	v_cmp_eq_u32_e64 s[10:11], 0, v5
	v_xor_b32_e32 v5, 16, v228
	v_cmp_lt_i32_e32 vcc, v5, v4
	v_lshlrev_b32_e32 v3, 5, v3
	s_mov_b32 s2, 0
	v_cndmask_b32_e32 v5, v228, v5, vcc
	v_lshlrev_b32_e32 v137, 2, v5
	v_and_b32_e32 v5, 8, v2
	v_cmp_eq_u32_e64 s[12:13], 0, v5
	v_xor_b32_e32 v5, 8, v228
	v_cmp_lt_i32_e32 vcc, v5, v4
	v_cmp_eq_u32_e64 s[6:7], 0, v133
	s_lshl_b32 s3, s97, 7
	v_cndmask_b32_e32 v4, v228, v5, vcc
	v_lshlrev_b32_e32 v138, 2, v4
	v_and_b32_e32 v4, 4, v2
	v_cmp_eq_u32_e64 s[14:15], 0, v4
	v_and_b32_e32 v4, 2, v2
	v_cmp_eq_u32_e64 s[16:17], 0, v4
	v_and_b32_e32 v4, 1, v2
	v_or_b32_e32 v2, s20, v132
	v_cmp_eq_u32_e64 s[18:19], 0, v4
	v_lshlrev_b32_e32 v126, 1, v2
	s_or_b32 s34, s20, 7
	s_lshl_b32 s42, s97, 6
	v_add_u32_e32 v139, 0, v3
	v_mov_b32_e32 v140, 0x358637bd
	s_mov_b32 s43, 0xf800000
	v_mov_b32_e32 v141, 0x260
	v_mov_b32_e32 v142, 1
	v_mov_b32_e32 v143, 0xff800000
	s_branch .LBB0_1407

; template <int layer> __device__ __forceinline__ void layer_phases(const Ctx& c, unsigned char* lds) {
;     ...
;                 const int npan_f = PANE[MAXPAN]; int npf_f = ((npan_f * 4) / G) * G / 4; if (npan_f - npf_f > 8 || npf_f == 0) npf_f = npan_f; const int tail0 = npf_f * 256;
;                 f32x4 gfv[4];
; #pragma unroll
;                 for (int j = 0; j < 4; ++j) gfv[j] = ((const f32x4*)args.g_final)[lane + 64 * j];
;                 int ppn[2][2];
; #pragma unroll
;                 for (int r = 0; r < 2; ++r) { const int m = gw + r * NGW; const int mc = m < M ? m : 0; ppn[r][0] = POS[mc * 2]; ppn[r][1] = POS[mc * 2 + 1]; }
.LBB0_1905:
	v_readlane_b32 s8, v254, 0
	s_cmp_lt_i32 s8, 28
	s_cselect_b64 s[2:3], -1, 0
	s_and_b64 s[2:3], s[2:3], s[4:5]
	s_andn2_b64 vcc, exec, s[2:3]
	v_readlane_b32 s9, v254, 1
	v_readlane_b32 s10, v254, 2
	v_readlane_b32 s11, v254, 3
	s_cbranch_vccnz .LBB0_1927
	s_waitcnt vmcnt(0)
	v_mov_b32_e32 v49, 0
	global_load_dword v120, v49, s[12:13]
	s_abs_i32 s3, s97
	v_cvt_f32_u32_e32 v121, s3
	v_readlane_b32 s4, v254, 46
	v_readlane_b32 s5, v254, 47
	s_andn2_b64 vcc, exec, s[4:5]
	v_rcp_iflag_f32_e32 v121, v121
	v_readlane_b32 s14, v254, 44
	s_add_i32 s17, s33, s14
	s_lshl_b32 s16, s17, 1
	s_cmpk_lt_i32 s17, 0x4000
	s_cselect_b32 s16, s16, 0
	s_cselect_b32 s31, s17, 0
	s_ashr_i32 s17, s16, 31
	s_lshl_b64 s[16:17], s[16:17], 2
	s_add_u32 s16, s0, s16
	s_addc_u32 s17, s1, s17
	s_lshl_b32 s24, s14, 1
	s_ashr_i32 s25, s24, 31
	s_lshl_b64 s[24:25], s[24:25], 2
	s_add_u32 s24, s0, s24
	s_addc_u32 s25, s1, s25
	v_and_b32_e32 v20, 63, v0
	v_lshlrev_b32_e32 v48, 4, v20
	global_load_dwordx2 v[16:17], v49, s[16:17]
	global_load_dwordx2 v[18:19], v49, s[24:25]
	global_load_dwordx4 v[0:3], v48, s[74:75]
	global_load_dwordx4 v[4:7], v48, s[74:75] offset:1024
	global_load_dwordx4 v[8:11], v48, s[74:75] offset:2048
	global_load_dwordx4 v[12:15], v48, s[74:75] offset:3072
	s_waitcnt vmcnt(6)
	v_readfirstlane_b32 s2, v120
	v_mul_f32_e32 v121, 0x4f7ffffe, v121
	v_cvt_u32_f32_e32 v121, v121
	s_nop 0
	v_readfirstlane_b32 s4, v121
	s_cbranch_vccnz .LBB0_1927
	s_sub_i32 s8, 0, s3
	s_mul_i32 s8, s8, s4
	s_lshl_b32 s5, s2, 2
	s_mul_hi_u32 s8, s4, s8
	s_abs_i32 s7, s5
	s_add_i32 s4, s4, s8
	s_mul_hi_u32 s4, s7, s4
	s_mul_i32 s4, s4, s3
	s_sub_i32 s4, s7, s4
	s_bfe_i32 s6, s2, 0x1001d
	s_sub_i32 s7, s4, s3
	s_cmp_ge_u32 s4, s3
	s_cselect_b32 s4, s7, s4
	s_sub_i32 s7, s4, s3
	s_cmp_ge_u32 s4, s3
	s_cselect_b32 s3, s7, s4
	s_xor_b32 s3, s3, s6
	s_sub_i32 s3, s6, s3
	s_add_i32 s3, s5, s3
	s_ashr_i32 s4, s3, 31
	s_lshr_b32 s4, s4, 30
	s_add_i32 s4, s3, s4
	s_ashr_i32 s8, s4, 2
	s_sub_i32 s4, s2, s8
	s_cmp_gt_i32 s4, 8
	s_cselect_b64 s[4:5], -1, 0
	s_add_i32 s3, s3, 3
	s_cmp_lt_u32 s3, 7
	s_cselect_b64 s[6:7], -1, 0
	s_or_b64 s[4:5], s[6:7], s[4:5]
	s_and_b64 s[4:5], s[4:5], exec
	s_cselect_b32 s2, s2, s8
	s_lshl_b32 s30, s2, 8
	v_and_b32_e32 v22, 64, v228
	v_xor_b32_e32 v24, 1, v228
	v_add_u32_e32 v30, 64, v22
	v_readlane_b32 s15, v254, 45
	s_mov_b64 s[4:5], 0x4c00000
	v_xor_b32_e32 v25, 2, v228
	v_readlane_b32 s10, v254, 29
	v_lshl_add_u64 v[22:23], s[78:79], 0, v[48:49]
	v_cmp_lt_i32_e32 vcc, v24, v30
	v_mov_b32_e32 v21, v49
	v_xor_b32_e32 v26, 4, v228
	v_lshlrev_b32_e32 v20, 3, v20
	v_readlane_b32 s11, v254, 30
	v_cndmask_b32_e32 v24, v228, v24, vcc
	v_cmp_lt_i32_e32 vcc, v25, v30
	v_lshl_add_u64 v[56:57], v[22:23], 0, s[4:5]
	s_ashr_i32 s83, s82, 31
	s_lshl_b64 s[4:5], s[14:15], 12
	v_xor_b32_e32 v27, 8, v228
	v_lshl_add_u64 v[52:53], s[10:11], 0, v[20:21]
	v_cndmask_b32_e32 v25, v228, v25, vcc
	v_cmp_lt_i32_e32 vcc, v26, v30
	s_add_u32 s10, s76, s4
	v_xor_b32_e32 v28, 16, v228
	v_cndmask_b32_e32 v26, v228, v26, vcc
	v_cmp_lt_i32_e32 vcc, v27, v30
	s_addc_u32 s11, s77, s5
	s_lshl_b64 s[4:5], s[82:83], 12
	s_lshl_b64 s[12:13], s[14:15], 11
	v_xor_b32_e32 v29, 32, v228
	v_cndmask_b32_e32 v27, v228, v27, vcc
	v_cmp_lt_i32_e32 vcc, v28, v30
	v_lshl_add_u64 v[22:23], s[10:11], 0, v[48:49]
	s_add_u32 s10, s78, s12
	v_cndmask_b32_e32 v28, v228, v28, vcc
	v_cmp_lt_i32_e32 vcc, v29, v30
	s_addc_u32 s11, s79, s13
	s_mov_b64 s[6:7], 0xc00
	s_mov_b64 s[8:9], 0x1aa00000
	v_lshl_add_u64 v[50:51], s[86:87], 0, v[20:21]
	v_cndmask_b32_e32 v29, v228, v29, vcc
	s_add_i32 s2, s94, s97
	v_readlane_b32 s42, v254, 10
	v_lshl_add_u64 v[20:21], s[10:11], 0, v[20:21]
	s_mov_b32 s3, 0
	s_mov_b32 s34, 0x800000
	s_mov_b32 s35, 0x1000000
	s_mov_b32 s36, 0x1800000
	v_mov_b32_e32 v94, 0x358637bd
	v_lshl_add_u64 v[54:55], s[76:77], 0, v[48:49]
	v_lshlrev_b32_e32 v95, 2, v24
	v_lshlrev_b32_e32 v96, 2, v25
	v_lshlrev_b32_e32 v97, 2, v26
	v_lshlrev_b32_e32 v98, 2, v27
	v_lshlrev_b32_e32 v99, 2, v28
	v_lshlrev_b32_e32 v100, 2, v29
	v_lshl_add_u64 v[58:59], v[22:23], 0, s[6:7]
	s_lshl_b64 s[6:7], s[82:83], 11
	s_add_i32 s37, s93, s42
	s_add_i32 s38, s82, s42
	s_lshl_b32 s39, s2, 3
	v_lshl_add_u64 v[60:61], v[20:21], 0, s[8:9]
	s_mov_b64 s[8:9], s[14:15]
	s_waitcnt vmcnt(5)
	v_readfirstlane_b32 s16, v16
	v_readfirstlane_b32 s17, v17
	s_waitcnt vmcnt(4)
	v_readfirstlane_b32 s24, v18
	v_readfirstlane_b32 s25, v19
	s_branch .LBB0_1910
